# prologue modulation GEMV: weight loads and their address arithmetic issued before the LDS reads of each iteration
# baseline (speedup 1.0000x reference)
; __device__ __forceinline__ void p0_prologue(const Args& a, const int wv) {
;     ...
;             for (int k = 0; k < 256; ++k) { const float wv = w[(size_t)k * 6144];
; #pragma unroll
;                 for (int b = 0; b < NBATCH; ++b) acc[b] += cs[b * DM + ksl * 256 + k] * wv; }
.LBB0_16:
	v_lshl_add_u64 v[122:123], v[112:113], 0, s[16:17]
	v_add_co_u32_e64 v154, s[2:3], s9, v122
	s_nop 1
	v_addc_co_u32_e64 v155, s[2:3], 0, v123, s[2:3]
	v_add_co_u32_e64 v156, s[2:3], s11, v122
	s_nop 1
	v_addc_co_u32_e64 v157, s[2:3], 0, v123, s[2:3]
	v_add_co_u32_e64 v158, s[2:3], s22, v122
	s_nop 1
	v_addc_co_u32_e64 v159, s[2:3], 0, v123, s[2:3]
	v_add_co_u32_e64 v160, s[2:3], s23, v122
	s_nop 1
	v_addc_co_u32_e64 v161, s[2:3], 0, v123, s[2:3]
	v_add_co_u32_e64 v162, s[2:3], s26, v122
	s_nop 1
	v_addc_co_u32_e64 v163, s[2:3], 0, v123, s[2:3]
	v_add_co_u32_e64 v164, s[2:3], s27, v122
	s_nop 1
	v_addc_co_u32_e64 v165, s[2:3], 0, v123, s[2:3]
	v_add_co_u32_e64 v166, s[2:3], s33, v122
	s_nop 1
	v_addc_co_u32_e64 v167, s[2:3], 0, v123, s[2:3]
	v_add_co_u32_e64 v168, s[2:3], s36, v122
	s_nop 1
	v_addc_co_u32_e64 v169, s[2:3], 0, v123, s[2:3]
	v_add_co_u32_e64 v170, s[2:3], s37, v122
	s_nop 1
	v_addc_co_u32_e64 v171, s[2:3], 0, v123, s[2:3]
	v_add_co_u32_e64 v172, s[2:3], s38, v122
	s_nop 1
	v_addc_co_u32_e64 v173, s[2:3], 0, v123, s[2:3]
	v_add_co_u32_e64 v174, s[2:3], s39, v122
	s_nop 1
	v_addc_co_u32_e64 v175, s[2:3], 0, v123, s[2:3]
	v_add_co_u32_e64 v176, s[2:3], s40, v122
	s_nop 1
	v_addc_co_u32_e64 v177, s[2:3], 0, v123, s[2:3]
	v_add_co_u32_e64 v178, s[2:3], s41, v122
	s_nop 1
	v_addc_co_u32_e64 v179, s[2:3], 0, v123, s[2:3]
	v_add_co_u32_e64 v180, s[2:3], s42, v122
	s_nop 1
	v_addc_co_u32_e64 v181, s[2:3], 0, v123, s[2:3]
	v_add_co_u32_e64 v182, s[2:3], s43, v122
	s_nop 1
	v_addc_co_u32_e64 v183, s[2:3], 0, v123, s[2:3]
	global_load_dword v122, v[122:123], off
	s_nop 0
	global_load_dword v154, v[154:155], off
	s_nop 0
	global_load_dword v156, v[156:157], off
	s_nop 0
	global_load_dword v158, v[158:159], off
	s_nop 0
	global_load_dword v160, v[160:161], off
	s_nop 0
	global_load_dword v162, v[162:163], off
	s_nop 0
	global_load_dword v164, v[164:165], off
	s_nop 0
	global_load_dword v166, v[166:167], off
	s_nop 0
	global_load_dword v168, v[168:169], off
	s_nop 0
	global_load_dword v170, v[170:171], off
	s_nop 0
	global_load_dword v172, v[172:173], off
	s_nop 0
	global_load_dword v174, v[174:175], off
	s_nop 0
	global_load_dword v176, v[176:177], off
	s_nop 0
	global_load_dword v178, v[178:179], off
	s_nop 0
	global_load_dword v180, v[180:181], off
	s_nop 0
	global_load_dword v182, v[182:183], off
	s_nop 0
	ds_read_b128 v[16:19], v129
	ds_read_b128 v[12:15], v129 offset:16
	ds_read_b128 v[8:11], v129 offset:32
	ds_read_b128 v[4:7], v129 offset:48
	ds_read_b128 v[0:3], v129 offset:4096
	ds_read_b128 v[20:23], v129 offset:4112
	ds_read_b128 v[60:63], v129 offset:8192
	ds_read_b128 v[52:55], v129 offset:8208
	ds_read_b128 v[32:35], v129 offset:12288
	ds_read_b128 v[24:27], v129 offset:12304
	ds_read_b128 v[68:71], v129 offset:16384
	ds_read_b128 v[56:59], v129 offset:16400
	ds_read_b128 v[40:43], v129 offset:20480
	ds_read_b128 v[28:31], v129 offset:20496
	ds_read_b128 v[72:75], v129 offset:24576
	ds_read_b128 v[64:67], v129 offset:24592
	ds_read_b128 v[44:47], v129 offset:28672
	ds_read_b128 v[36:39], v129 offset:28688
	ds_read_b128 v[48:51], v129 offset:4128
	ds_read_b128 v[76:79], v129 offset:4144
	ds_read_b128 v[130:133], v129 offset:8224
	ds_read_b128 v[134:137], v129 offset:8240
	ds_read_b128 v[88:91], v129 offset:12320
	ds_read_b128 v[80:83], v129 offset:12336
	ds_read_b128 v[138:141], v129 offset:16416
	ds_read_b128 v[142:145], v129 offset:16432
	ds_read_b128 v[96:99], v129 offset:20512
	ds_read_b128 v[84:87], v129 offset:20528
	ds_read_b128 v[146:149], v129 offset:24608
	ds_read_b128 v[150:153], v129 offset:24624
	ds_read_b128 v[100:103], v129 offset:28704
	ds_read_b128 v[92:95], v129 offset:28720
	s_waitcnt lgkmcnt(14)
	v_mov_b32_e32 v184, v16
	v_mov_b32_e32 v185, v0
	v_mov_b32_e32 v186, v60
	v_mov_b32_e32 v187, v32
	v_mov_b32_e32 v188, v68
	v_mov_b32_e32 v189, v40
	v_mov_b32_e32 v190, v72
	v_mov_b32_e32 v191, v44
	v_mov_b32_e32 v0, v17
	v_mov_b32_e32 v32, v61
	v_mov_b32_e32 v40, v69
	v_mov_b32_e32 v44, v73
	v_mov_b32_e32 v16, v18
	v_mov_b32_e32 v17, v2
	v_mov_b32_e32 v2, v19
	v_mov_b32_e32 v18, v12
	v_mov_b32_e32 v19, v20
	v_mov_b32_e32 v20, v13
	v_mov_b32_e32 v12, v14
	v_mov_b32_e32 v13, v22
	v_mov_b32_e32 v22, v15
	v_mov_b32_e32 v14, v8
	s_waitcnt lgkmcnt(13)
	v_mov_b32_e32 v15, v48
	v_mov_b32_e32 v48, v9
	v_mov_b32_e32 v8, v10
	v_mov_b32_e32 v9, v50
	v_mov_b32_e32 v50, v11
	v_mov_b32_e32 v10, v4
	s_waitcnt lgkmcnt(12)
	v_mov_b32_e32 v11, v76
	v_mov_b32_e32 v76, v5
	v_mov_b32_e32 v4, v6
	v_mov_b32_e32 v5, v78
	v_mov_b32_e32 v78, v7
	v_mov_b32_e32 v60, v62
	v_mov_b32_e32 v61, v34
	v_mov_b32_e32 v68, v70
	v_mov_b32_e32 v69, v42
	v_mov_b32_e32 v72, v74
	v_mov_b32_e32 v73, v46
	v_mov_b32_e32 v34, v63
	v_mov_b32_e32 v42, v71
	v_mov_b32_e32 v46, v75
	v_mov_b32_e32 v62, v52
	v_mov_b32_e32 v63, v24
	v_mov_b32_e32 v70, v56
	v_mov_b32_e32 v71, v28
	v_mov_b32_e32 v74, v64
	v_mov_b32_e32 v75, v36
	v_mov_b32_e32 v24, v53
	v_mov_b32_e32 v28, v57
	v_mov_b32_e32 v36, v65
	v_mov_b32_e32 v52, v54
	v_mov_b32_e32 v53, v26
	v_mov_b32_e32 v56, v58
	v_mov_b32_e32 v57, v30
	v_mov_b32_e32 v64, v66
	v_mov_b32_e32 v65, v38
	v_mov_b32_e32 v26, v55
	v_mov_b32_e32 v30, v59
	v_mov_b32_e32 v38, v67
	s_waitcnt lgkmcnt(11)
	v_mov_b32_e32 v54, v130
	s_waitcnt lgkmcnt(9)
	v_mov_b32_e32 v55, v88
	s_waitcnt lgkmcnt(7)
	v_mov_b32_e32 v58, v138
	s_waitcnt lgkmcnt(5)
	v_mov_b32_e32 v59, v96
	s_waitcnt lgkmcnt(3)
	v_mov_b32_e32 v66, v146
	s_waitcnt lgkmcnt(1)
	v_mov_b32_e32 v67, v100
	v_mov_b32_e32 v88, v131
	v_mov_b32_e32 v96, v139
	v_mov_b32_e32 v100, v147
	v_mov_b32_e32 v130, v132
	v_mov_b32_e32 v131, v90
	v_mov_b32_e32 v138, v140
	v_mov_b32_e32 v139, v98
	v_mov_b32_e32 v146, v148
	v_mov_b32_e32 v147, v102
	v_mov_b32_e32 v90, v133
	v_mov_b32_e32 v98, v141
	v_mov_b32_e32 v102, v149
	s_waitcnt vmcnt(15)
; __device__ __forceinline__ void p0_prologue(const Args& a, const int wv) {
;     ...
;             for (int k = 0; k < 256; ++k) { const float wv = w[(size_t)k * 6144];
; #pragma unroll
;                 for (int b = 0; b < NBATCH; ++b) acc[b] += cs[b * DM + ksl * 256 + k] * wv; }
; #pragma unroll
;             for (int b = 0; b < NBATCH; ++b) red[(ksl * NBATCH + b) * 128 + (F.tid & 127)] = acc[b];
;             __syncthreads();
;             for (int o = F.tid; o < NBATCH * 128; o += 512) { const int b = o >> 7, nn = o & 127;
;                 const float s = red[(0 * NBATCH + b) * 128 + nn] + red[(1 * NBATCH + b) * 128 + nn] + red[(2 * NBATCH + b) * 128 + nn] + red[(3 * NBATCH + b) * 128 + nn];
;                 const int col = (it % 48) * 128 + nn;
;                 mod[((size_t)l * NBATCH + b) * 6144 + col] = s + a.ada_b[(size_t)l * 6144 + col]; }
	v_pk_fma_f32 v[6:7], v[122:123], v[184:185], v[116:117] op_sel_hi:[0,1,1]
	v_pk_fma_f32 v[116:117], v[122:123], v[186:187], v[118:119] op_sel_hi:[0,1,1]
	v_pk_fma_f32 v[118:119], v[122:123], v[188:189], v[120:121] op_sel_hi:[0,1,1]
	v_pk_fma_f32 v[114:115], v[122:123], v[190:191], v[114:115] op_sel_hi:[0,1,1]
	s_waitcnt vmcnt(14)
	v_pk_fma_f32 v[0:1], v[154:155], v[0:1], v[6:7] op_sel_hi:[0,1,1]
	v_pk_fma_f32 v[6:7], v[154:155], v[32:33], v[116:117] op_sel_hi:[0,1,1]
	v_pk_fma_f32 v[32:33], v[154:155], v[40:41], v[118:119] op_sel_hi:[0,1,1]
	v_pk_fma_f32 v[40:41], v[154:155], v[44:45], v[114:115] op_sel_hi:[0,1,1]
	s_waitcnt vmcnt(13)
	v_pk_fma_f32 v[0:1], v[156:157], v[16:17], v[0:1] op_sel_hi:[0,1,1]
	v_pk_fma_f32 v[6:7], v[156:157], v[60:61], v[6:7] op_sel_hi:[0,1,1]
	v_pk_fma_f32 v[16:17], v[156:157], v[68:69], v[32:33] op_sel_hi:[0,1,1]
	v_pk_fma_f32 v[32:33], v[156:157], v[72:73], v[40:41] op_sel_hi:[0,1,1]
	s_waitcnt vmcnt(12)
	v_pk_fma_f32 v[0:1], v[158:159], v[2:3], v[0:1] op_sel_hi:[0,1,1]
	v_pk_fma_f32 v[2:3], v[158:159], v[34:35], v[6:7] op_sel_hi:[0,1,1]
	v_pk_fma_f32 v[6:7], v[158:159], v[42:43], v[16:17] op_sel_hi:[0,1,1]
	v_pk_fma_f32 v[16:17], v[158:159], v[46:47], v[32:33] op_sel_hi:[0,1,1]
	s_waitcnt vmcnt(11)
	v_pk_fma_f32 v[0:1], v[160:161], v[18:19], v[0:1] op_sel_hi:[0,1,1]
	v_pk_fma_f32 v[2:3], v[160:161], v[62:63], v[2:3] op_sel_hi:[0,1,1]
	v_pk_fma_f32 v[6:7], v[160:161], v[70:71], v[6:7] op_sel_hi:[0,1,1]
	v_pk_fma_f32 v[16:17], v[160:161], v[74:75], v[16:17] op_sel_hi:[0,1,1]
	s_waitcnt vmcnt(10)
	v_pk_fma_f32 v[0:1], v[162:163], v[20:21], v[0:1] op_sel_hi:[0,1,1]
	v_pk_fma_f32 v[2:3], v[162:163], v[24:25], v[2:3] op_sel_hi:[0,1,1]
	v_pk_fma_f32 v[6:7], v[162:163], v[28:29], v[6:7] op_sel_hi:[0,1,1]
	v_pk_fma_f32 v[16:17], v[162:163], v[36:37], v[16:17] op_sel_hi:[0,1,1]
	s_waitcnt vmcnt(9)
	v_pk_fma_f32 v[0:1], v[164:165], v[12:13], v[0:1] op_sel_hi:[0,1,1]
	v_pk_fma_f32 v[2:3], v[164:165], v[52:53], v[2:3] op_sel_hi:[0,1,1]
	v_pk_fma_f32 v[6:7], v[164:165], v[56:57], v[6:7] op_sel_hi:[0,1,1]
	v_pk_fma_f32 v[12:13], v[164:165], v[64:65], v[16:17] op_sel_hi:[0,1,1]
	s_waitcnt vmcnt(8)
	v_pk_fma_f32 v[0:1], v[166:167], v[22:23], v[0:1] op_sel_hi:[0,1,1]
	v_pk_fma_f32 v[2:3], v[166:167], v[26:27], v[2:3] op_sel_hi:[0,1,1]
	v_pk_fma_f32 v[6:7], v[166:167], v[30:31], v[6:7] op_sel_hi:[0,1,1]
	v_pk_fma_f32 v[12:13], v[166:167], v[38:39], v[12:13] op_sel_hi:[0,1,1]
	s_waitcnt vmcnt(7)
	v_pk_fma_f32 v[0:1], v[168:169], v[14:15], v[0:1] op_sel_hi:[0,1,1]
	v_pk_fma_f32 v[2:3], v[168:169], v[54:55], v[2:3] op_sel_hi:[0,1,1]
	v_pk_fma_f32 v[6:7], v[168:169], v[58:59], v[6:7] op_sel_hi:[0,1,1]
	v_pk_fma_f32 v[12:13], v[168:169], v[66:67], v[12:13] op_sel_hi:[0,1,1]
	s_waitcnt vmcnt(6)
	v_pk_fma_f32 v[0:1], v[170:171], v[48:49], v[0:1] op_sel_hi:[0,1,1]
	v_pk_fma_f32 v[2:3], v[170:171], v[88:89], v[2:3] op_sel_hi:[0,1,1]
	v_pk_fma_f32 v[6:7], v[170:171], v[96:97], v[6:7] op_sel_hi:[0,1,1]
	v_pk_fma_f32 v[12:13], v[170:171], v[100:101], v[12:13] op_sel_hi:[0,1,1]
	s_waitcnt vmcnt(5)
	v_pk_fma_f32 v[0:1], v[172:173], v[8:9], v[0:1] op_sel_hi:[0,1,1]
	v_pk_fma_f32 v[2:3], v[172:173], v[130:131], v[2:3] op_sel_hi:[0,1,1]
	v_pk_fma_f32 v[6:7], v[172:173], v[138:139], v[6:7] op_sel_hi:[0,1,1]
	v_pk_fma_f32 v[8:9], v[172:173], v[146:147], v[12:13] op_sel_hi:[0,1,1]
	v_mov_b32_e32 v132, v134
	v_mov_b32_e32 v133, v80
	v_mov_b32_e32 v140, v142
	v_mov_b32_e32 v141, v84
	v_mov_b32_e32 v148, v150
	s_waitcnt lgkmcnt(0)
	v_mov_b32_e32 v149, v92
	s_waitcnt vmcnt(4)
	v_pk_fma_f32 v[0:1], v[174:175], v[50:51], v[0:1] op_sel_hi:[0,1,1]
	v_pk_fma_f32 v[2:3], v[174:175], v[90:91], v[2:3] op_sel_hi:[0,1,1]
	v_pk_fma_f32 v[6:7], v[174:175], v[98:99], v[6:7] op_sel_hi:[0,1,1]
	v_pk_fma_f32 v[8:9], v[174:175], v[102:103], v[8:9] op_sel_hi:[0,1,1]
	v_mov_b32_e32 v80, v135
	v_mov_b32_e32 v84, v143
	v_mov_b32_e32 v92, v151
	s_waitcnt vmcnt(3)
	v_pk_fma_f32 v[0:1], v[176:177], v[10:11], v[0:1] op_sel_hi:[0,1,1]
	v_pk_fma_f32 v[2:3], v[176:177], v[132:133], v[2:3] op_sel_hi:[0,1,1]
	v_pk_fma_f32 v[6:7], v[176:177], v[140:141], v[6:7] op_sel_hi:[0,1,1]
	v_pk_fma_f32 v[8:9], v[176:177], v[148:149], v[8:9] op_sel_hi:[0,1,1]
	s_add_u32 s16, s16, 0x60000
	v_mov_b32_e32 v134, v136
	v_mov_b32_e32 v135, v82
	v_mov_b32_e32 v142, v144
	v_mov_b32_e32 v143, v86
	v_mov_b32_e32 v150, v152
	v_mov_b32_e32 v151, v94
	s_waitcnt vmcnt(2)
	v_pk_fma_f32 v[0:1], v[178:179], v[76:77], v[0:1] op_sel_hi:[0,1,1]
	v_pk_fma_f32 v[2:3], v[178:179], v[80:81], v[2:3] op_sel_hi:[0,1,1]
	v_pk_fma_f32 v[6:7], v[178:179], v[84:85], v[6:7] op_sel_hi:[0,1,1]
	v_pk_fma_f32 v[8:9], v[178:179], v[92:93], v[8:9] op_sel_hi:[0,1,1]
	s_addc_u32 s17, s17, 0
	v_mov_b32_e32 v82, v137
	v_mov_b32_e32 v86, v145
	v_mov_b32_e32 v94, v153
	s_waitcnt vmcnt(1)
	v_pk_fma_f32 v[0:1], v[180:181], v[4:5], v[0:1] op_sel_hi:[0,1,1]
	v_pk_fma_f32 v[2:3], v[180:181], v[134:135], v[2:3] op_sel_hi:[0,1,1]
	v_pk_fma_f32 v[4:5], v[180:181], v[142:143], v[6:7] op_sel_hi:[0,1,1]
	v_pk_fma_f32 v[6:7], v[180:181], v[150:151], v[8:9] op_sel_hi:[0,1,1]
	v_add_u32_e32 v129, 64, v129
	s_cmp_eq_u32 s16, 0x600000
	s_waitcnt vmcnt(0)
	v_pk_fma_f32 v[116:117], v[182:183], v[78:79], v[0:1] op_sel_hi:[0,1,1]
	v_pk_fma_f32 v[118:119], v[182:183], v[82:83], v[2:3] op_sel_hi:[0,1,1]
	v_pk_fma_f32 v[120:121], v[182:183], v[86:87], v[4:5] op_sel_hi:[0,1,1]
	v_pk_fma_f32 v[114:115], v[182:183], v[94:95], v[6:7] op_sel_hi:[0,1,1]
	s_cbranch_scc0 .LBB0_16
	ds_write2st64_b32 v127, v116, v117 offset0:128 offset1:130
	ds_write2st64_b32 v127, v118, v119 offset0:132 offset1:134
	ds_write2st64_b32 v127, v120, v121 offset0:136 offset1:138
	ds_write2st64_b32 v127, v114, v115 offset0:140 offset1:142
	s_waitcnt lgkmcnt(0)
	s_barrier
	s_and_saveexec_b64 s[16:17], vcc
	s_cbranch_execz .LBB0_14
	s_load_dwordx2 s[2:3], s[4:5], 0x20
	s_mul_i32 s21, s14, 0x6000
	s_mul_hi_i32 s20, s14, 0x6000
	v_lshlrev_b64 v[2:3], 2, v[110:111]
	v_mov_b32_e32 v4, v128
	s_waitcnt lgkmcnt(0)
	s_add_u32 s2, s2, s21
	s_addc_u32 s3, s3, s20
	s_lshl_b64 s[14:15], s[14:15], 3
	v_lshl_add_u64 v[0:1], s[2:3], 0, v[2:3]
	v_lshl_add_u64 v[2:3], s[12:13], 0, v[2:3]
	s_mov_b64 s[20:21], 0
	v_mov_b32_e32 v5, v108
